# baseline (speedup 1.0000x reference)
_Z11knrm_kernelPKfS0_PKiS2_S0_Pf:
	s_setprio 3
	s_load_dwordx8 s[4:11], s[0:1], 0x0
	s_load_dwordx4 s[12:15], s[0:1], 0x20
	v_lshrrev_b32_e32 v1, 6, v0
	v_and_b32_e32 v120, 63, v0
	v_lshrrev_b32_e32 v100, 4, v0
	v_and_b32_e32 v123, 15, v0
	v_lshlrev_b32_e32 v124, 5, v1
	s_lshl_b32 s3, s2, 5
	v_lshl_or_b32 v8, s2, 8, v124
	v_or_b32_e32 v2, s3, v100
	s_movk_i32 s3, 0x4b0
	v_mul_lo_u32 v2, v2, s3
	v_mul_lo_u32 v99, v8, s3
	v_lshlrev_b32_e32 v132, 4, v120
	v_min_u32_e32 v193, 23, v120
	v_lshl_add_u32 v3, v123, 4, v2
	v_min_u32_e32 v4, 10, v123
	v_add_u32_e32 v192, v99, v132
	v_lshlrev_b32_e32 v193, 4, v193
	s_movk_i32 s27, 0x1000
	s_movk_i32 s28, 0x2000
	v_lshl_add_u32 v2, v4, 4, v2
	v_add3_u32 v193, v99, v193, s28
	s_mov_b32 s19, 0x20000
	s_mov_b32 s18, 0x4b00000
	s_waitcnt lgkmcnt(0)
	s_mov_b64 s[16:17], s[6:7]
	s_and_b32 s5, s5, 0xffff
	s_mov_b32 s6, 0x960000
	s_mov_b32 s7, s19
	s_and_b32 s17, s17, 0xffff
	buffer_load_dwordx4 v[90:93], v3, s[4:7], 0 offen nt
	buffer_load_dwordx4 v[86:89], v3, s[4:7], 0 offen offset:256 nt
	buffer_load_dwordx4 v[82:85], v3, s[4:7], 0 offen offset:512 nt
	buffer_load_dwordx4 v[78:81], v3, s[4:7], 0 offen offset:768 nt
	buffer_load_dwordx4 v[94:97], v2, s[4:7], 0 offen offset:1024 nt
	buffer_load_dwordx4 v[2:5], v192, s[16:19], 0 offen nt
	buffer_load_dwordx4 v[14:17], v192, s[16:19], 0 offen offset:1024 nt
	buffer_load_dwordx4 v[34:37], v192, s[16:19], 0 offen offset:2048 nt
	buffer_load_dwordx4 v[46:49], v192, s[16:19], 0 offen offset:3072 nt
	buffer_load_dwordx4 v[54:57], v192, s[16:19], s27 offen nt
	buffer_load_dwordx4 v[58:61], v192, s[16:19], s27 offen offset:1024 nt
	buffer_load_dwordx4 v[62:65], v192, s[16:19], s27 offen offset:2048 nt
	buffer_load_dwordx4 v[66:69], v192, s[16:19], s27 offen offset:3072 nt
	buffer_load_dwordx4 v[70:73], v192, s[16:19], s28 offen nt
	buffer_load_dwordx4 v[74:77], v193, s[16:19], 0 offen offset:1024 nt
	v_lshlrev_b32_e32 v42, 2, v0
	v_bfe_u32 v43, v0, 2, 2
	v_and_or_b32 v98, v42, 12, v43
	v_and_or_b32 v6, v98, 7, v8
	v_ashrrev_i32_e32 v7, 31, v6
	s_movk_i32 s0, 0x160
	v_lshl_add_u64 v[6:7], v[6:7], 2, s[10:11]
	v_lshrrev_b32_e32 v121, 5, v0
	v_cmp_gt_u32_e64 s[0:1], s0, v0
	global_load_dword v125, v[6:7], off
	global_load_dword v126, v[6:7], off offset:64
	global_load_dword v127, v[6:7], off offset:96
	global_load_dword v190, v[6:7], off offset:32
	v_cndmask_b32_e64 v42, 10, v121, s[0:1]
	v_lshlrev_b32_e32 v42, 2, v42
	s_lshl_b32 s3, s2, 5
	v_and_b32_e32 v122, 31, v0
	global_load_dword v118, v42, s[12:13]
	v_or_b32_e32 v42, s3, v122
	v_ashrrev_i32_e32 v43, 31, v42
	v_lshl_add_u64 v[42:43], v[42:43], 2, s[8:9]
	global_load_dword v119, v[42:43], off
	s_mov_b32 s3, 0
	v_mul_u32_u24_e32 v131, 0x2600, v1
	v_cmp_gt_u32_e64 s[4:5], 16, v120
	s_and_saveexec_b64 s[6:7], s[4:5]
	s_movk_i32 s8, 0x260
	v_mov_b32_e32 v102, 0
	v_mad_u32_u24 v101, v120, s8, v131
	v_mov_b32_e32 v103, v102
	ds_write_b64 v101, v[102:103] offset:20056
	s_or_b64 exec, exec, s[6:7]
	v_cmp_lt_u32_e32 vcc, 10, v123
	s_waitcnt vmcnt(19)
	v_mul_f32_e32 v101, v87, v87
	v_mov_b32_e32 v106, v92
	s_waitcnt vmcnt(16)
	v_cndmask_b32_e64 v103, v97, 0, vcc
	v_cndmask_b32_e64 v102, v96, 0, vcc
	v_mov_b32_e32 v96, v91
	v_mov_b32_e32 v97, v83
	v_cndmask_b32_e64 v105, v95, 0, vcc
	v_cndmask_b32_e64 v104, v94, 0, vcc
	v_mov_b32_e32 v94, v90
	v_mov_b32_e32 v95, v82
	v_pk_mul_f32 v[96:97], v[96:97], v[96:97]
	v_mov_b32_e32 v107, v84
	v_fmac_f32_e32 v101, v86, v86
	v_pk_fma_f32 v[94:95], v[94:95], v[94:95], v[96:97]
	v_mov_b32_e32 v108, v93
	v_mov_b32_e32 v109, v85
	v_fmac_f32_e32 v101, v88, v88
	v_pk_fma_f32 v[94:95], v[106:107], v[106:107], v[94:95]
	v_fmac_f32_e32 v101, v89, v89
	v_pk_fma_f32 v[94:95], v[108:109], v[108:109], v[94:95]
	v_mov_b32_e32 v96, v79
	v_add_f32_e32 v94, v94, v101
	v_mov_b32_e32 v97, v105
	v_add_f32_e32 v101, v94, v95
	v_mov_b32_e32 v94, v78
	v_mov_b32_e32 v95, v104
	v_pk_mul_f32 v[96:97], v[96:97], v[96:97]
	s_mov_b32 s21, 0xf800000
	v_pk_fma_f32 v[94:95], v[94:95], v[94:95], v[96:97]
	v_mov_b32_e32 v96, v80
	v_mov_b32_e32 v97, v102
	v_pk_fma_f32 v[94:95], v[96:97], v[96:97], v[94:95]
	v_mov_b32_e32 v96, v81
	v_mov_b32_e32 v97, v103
	v_pk_fma_f32 v[94:95], v[96:97], v[96:97], v[94:95]
	v_mov_b32_e32 v135, 0x260
	v_add_f32_e32 v94, v101, v94
	v_add_f32_e32 v94, v94, v95
	v_mbcnt_lo_u32_b32 v95, -1, 0
	v_mbcnt_hi_u32_b32 v95, -1, v95
	v_and_b32_e32 v97, 64, v95
	v_add_u32_e32 v101, 64, v97
	s_movk_i32 s8, 0x260
	v_add_u32_e32 v137, 0x4b00, v99
	s_movk_i32 s10, 0x1b5
	v_mov_b32_e32 v99, 0x36a00
	v_mov_b32_e32 v111, 0x666c0
	v_mov_b32_e32 v113, 0x6d400
	v_mov_b32_e32 v115, 0x74140
	s_mov_b32 s20, 0xbeb17218
	s_mov_b32 s22, 0x44132d1f
	v_mov_b32_e32 v161, 0xc47a0000
	v_add_f32_dpp v96, v94, v94 quad_perm:[1,0,3,2] row_mask:0xf bank_mask:0xf
	s_nop 1
	v_add_f32_dpp v94, v96, v96 quad_perm:[2,3,0,1] row_mask:0xf bank_mask:0xf
	s_nop 1
	v_add_f32_dpp v96, v94, v94 row_half_mirror row_mask:0xf bank_mask:0xf
	s_nop 1
	v_add_f32_dpp v94, v96, v96 row_mirror row_mask:0xf bank_mask:0xf
	v_mul_f32_e32 v96, 0x4f800000, v94
	v_cmp_gt_f32_e32 vcc, s21, v94
	s_nop 1
	v_cndmask_b32_e32 v94, v94, v96, vcc
	v_sqrt_f32_e32 v96, v94
	s_nop 0
	v_add_u32_e32 v106, -1, v96
	v_fma_f32 v107, -v106, v96, v94
	v_cmp_ge_f32_e64 s[6:7], 0, v107
	v_add_u32_e32 v107, 1, v96
	s_nop 0
	v_cndmask_b32_e64 v106, v96, v106, s[6:7]
	v_fma_f32 v96, -v107, v96, v94
	v_cmp_lt_f32_e64 s[6:7], 0, v96
	s_nop 1
	v_cndmask_b32_e64 v96, v106, v107, s[6:7]
	v_mul_f32_e32 v106, 0x37800000, v96
	v_cndmask_b32_e32 v96, v96, v106, vcc
	v_cmp_class_f32_e32 vcc, v94, v135
	s_nop 1
	v_cndmask_b32_e32 v94, v96, v94, vcc
	v_add_f32_e32 v96, 0x29e12e13, v94
	v_div_scale_f32 v106, s[6:7], v96, v96, 1.0
	v_rcp_f32_e32 v107, v106
	v_mov_b32_e32 v94, 0
	v_cmp_gt_u32_e64 s[6:7], 48, v120
	v_mov_b32_e32 v116, v94
	v_fma_f32 v108, -v106, v107, 1.0
	v_fmac_f32_e32 v107, v108, v107
	v_div_scale_f32 v108, vcc, 1.0, v96, 1.0
	v_mul_f32_e32 v109, v108, v107
	v_fma_f32 v110, -v106, v109, v108
	v_fmac_f32_e32 v109, v110, v107
	v_fma_f32 v106, -v106, v109, v108
	v_div_fmas_f32 v106, v106, v107, v109
	v_div_fixup_f32 v96, v106, v96, 1.0
	v_lshlrev_b32_e32 v106, 3, v123
	v_pk_mul_f32 v[82:83], v[96:97], v[82:83] op_sel_hi:[0,1]
	v_pk_mul_f32 v[84:85], v[96:97], v[84:85] op_sel_hi:[0,1]
	v_pk_mul_f32 v[78:79], v[96:97], v[78:79] op_sel_hi:[0,1]
	v_pk_mul_f32 v[80:81], v[96:97], v[80:81] op_sel_hi:[0,1]
	v_mad_u32_u24 v100, v100, s8, v106
	v_cvt_pk_f16_f32 v82, v82, v83
	v_cvt_pk_f16_f32 v83, v84, v85
	v_cvt_pk_f16_f32 v78, v78, v79
	v_cvt_pk_f16_f32 v79, v80, v81
	ds_write2_b64 v100, v[82:83], v[78:79] offset0:32 offset1:48
	v_min_u32_e32 v82, 23, v120
	v_mov_b32_e32 v83, 0x2400
	v_lshl_or_b32 v138, v82, 4, v83
	v_xor_b32_e32 v83, 16, v95
	v_cmp_lt_i32_e32 vcc, v83, v101
	v_pk_mul_f32 v[90:91], v[96:97], v[90:91] op_sel_hi:[0,1]
	v_pk_mul_f32 v[92:93], v[96:97], v[92:93] op_sel_hi:[0,1]
	v_cndmask_b32_e32 v83, v95, v83, vcc
	v_lshlrev_b32_e32 v133, 2, v83
	v_xor_b32_e32 v83, 32, v95
	v_pk_mul_f32 v[86:87], v[96:97], v[86:87] op_sel_hi:[0,1]
	v_pk_mul_f32 v[88:89], v[96:97], v[88:89] op_sel_hi:[0,1]
	v_pk_mul_f32 v[78:79], v[96:97], v[104:105] op_sel_hi:[0,1]
	v_pk_mul_f32 v[80:81], v[96:97], v[102:103] op_sel_hi:[0,1]
	v_cmp_lt_i32_e32 vcc, v83, v101
	v_cvt_pk_f16_f32 v90, v90, v91
	v_cvt_pk_f16_f32 v91, v92, v93
	v_cvt_pk_f16_f32 v86, v86, v87
	v_cvt_pk_f16_f32 v87, v88, v89
	v_cvt_pk_f16_f32 v78, v78, v79
	v_cvt_pk_f16_f32 v79, v80, v81
	v_mov_b32_e32 v81, 0x17c00
	v_cndmask_b32_e32 v83, v95, v83, vcc
	ds_write2_b64 v100, v[90:91], v[86:87] offset1:16
	v_sub_u32_e64 v80, v123, 11 clamp
	v_lshl_or_b32 v81, v1, 7, v81
	v_lshlrev_b32_e32 v134, 2, v83
	v_or_b32_e32 v83, 64, v120
	v_mov_b32_e32 v86, 0x6d40
	v_mov_b32_e32 v87, 0xda80
	v_mov_b32_e32 v89, 0x147c0
	v_mov_b32_e32 v91, 0x1b500
	v_mov_b32_e32 v93, 0x28f80
	v_mov_b32_e32 v96, 0x2fcc0
	v_mov_b32_e32 v101, 0x3d740
	v_mov_b32_e32 v103, 0x44480
	v_mov_b32_e32 v105, 0x4b1c0
	v_mov_b32_e32 v107, 0x58c40
	v_or_b32_e32 v109, 0x3c0, v0
	v_mad_i32_i24 v80, v80, -8, v100
	v_lshrrev_b32_e32 v82, 1, v120
	v_lshl_add_u32 v139, v120, 2, v81
	v_and_or_b32 v140, v120, 48, v81
	v_lshlrev_b32_e32 v81, 3, v120
	v_mul_u32_u24_e32 v84, 0x1b5, v83
	v_lshl_add_u32 v85, v83, 3, v131
	v_mad_u32_u24 v86, v83, s10, v86
	v_mad_u32_u24 v87, v83, s10, v87
	v_mad_u32_u24 v89, v83, s10, v89
	v_mad_u32_u24 v91, v83, s10, v91
	v_mad_u32_u24 v93, v83, s10, v93
	v_mad_u32_u24 v96, v83, s10, v96
	v_mad_u32_u24 v99, v83, s10, v99
	v_mad_u32_u24 v101, v83, s10, v101
	v_mad_u32_u24 v103, v83, s10, v103
	v_mad_u32_u24 v105, v83, s10, v105
	v_mad_u32_u24 v107, v83, s10, v107
	v_mul_u32_u24_e32 v110, 0x1b5, v109
	v_mad_u32_u24 v111, v83, s10, v111
	v_mad_u32_u24 v113, v83, s10, v113
	v_mad_u32_u24 v83, v83, s10, v115
	ds_write_b64 v80, v[78:79] offset:512
	v_mul_u32_u24_e32 v78, 0x260, v123
	v_and_b32_e32 v82, 24, v82
	v_lshrrev_b32_e32 v84, 12, v84
	v_add_u32_e32 v141, v131, v81
	v_lshrrev_b32_e32 v86, 12, v86
	v_lshrrev_b32_e32 v87, 12, v87
	v_lshrrev_b32_e32 v89, 12, v89
	v_lshrrev_b32_e32 v91, 12, v91
	v_lshrrev_b32_e32 v93, 12, v93
	v_lshrrev_b32_e32 v96, 12, v96
	v_lshrrev_b32_e32 v99, 12, v99
	v_lshrrev_b32_e32 v101, 12, v101
	v_lshrrev_b32_e32 v103, 12, v103
	v_lshrrev_b32_e32 v105, 12, v105
	v_lshrrev_b32_e32 v107, 12, v107
	v_lshrrev_b32_e32 v110, 12, v110
	v_lshrrev_b32_e32 v111, 12, v111
	v_lshrrev_b32_e32 v113, 12, v113
	v_lshrrev_b32_e32 v83, 12, v83
	v_and_b32_e32 v79, 48, v0
	v_mad_u32_u24 v80, v98, s8, v131
	v_and_b32_e32 v84, 8, v84
	v_add_u32_e32 v81, 0x400, v141
	v_and_b32_e32 v86, 24, v86
	v_add_u32_e32 v88, 0x600, v141
	v_and_b32_e32 v87, 24, v87
	v_add_u32_e32 v90, 0x800, v141
	v_and_b32_e32 v89, 56, v89
	v_add_u32_e32 v92, 0xa00, v141
	v_and_b32_e32 v91, 56, v91
	v_add_u32_e32 v95, 0xe00, v141
	v_and_b32_e32 v93, 56, v93
	v_add_u32_e32 v98, 0x1000, v141
	v_and_b32_e32 v96, 56, v96
	v_add_u32_e32 v100, 0x1200, v141
	v_and_b32_e32 v99, 0x78, v99
	v_add_u32_e32 v102, 0x1400, v141
	v_and_b32_e32 v101, 0x78, v101
	v_add_u32_e32 v104, 0x1600, v141
	v_and_b32_e32 v103, 0x58, v103
	v_add_u32_e32 v106, 0x1800, v141
	v_and_b32_e32 v105, 0x58, v105
	v_add_u32_e32 v108, 0x1c00, v141
	v_and_b32_e32 v107, 0x78, v107
	v_lshl_add_u32 v109, v109, 3, v131
	v_and_b32_e32 v110, 0x78, v110
	v_add_u32_e32 v112, 0x2000, v141
	v_and_b32_e32 v111, 0x78, v111
	v_add_u32_e32 v114, 0x2200, v141
	v_and_b32_e32 v113, 0x78, v113
	v_add_u32_e32 v115, 0x2400, v141
	v_and_b32_e32 v83, 0xf8, v83
	s_movk_i32 s10, 0x4c00
	v_add_u32_e32 v78, v78, v82
	v_mad_u32_u24 v136, v123, s8, v79
	v_cmp_gt_u32_e64 s[8:9], 24, v120
	v_add3_u32 v142, v80, v79, s10
	v_add_u32_e32 v143, v85, v84
	v_add_u32_e32 v144, v81, v86
	v_add_u32_e32 v145, v88, v87
	v_add_u32_e32 v146, v90, v89
	v_add_u32_e32 v147, v92, v91
	v_add_u32_e32 v148, v95, v93
	v_add_u32_e32 v149, v98, v96
	v_add_u32_e32 v150, v100, v99
	v_add_u32_e32 v151, v102, v101
	v_add_u32_e32 v152, v104, v103
	v_add_u32_e32 v153, v106, v105
	v_add_u32_e32 v154, v108, v107
	v_add_u32_e32 v155, v109, v110
	v_add_u32_e32 v156, v112, v111
	v_add_u32_e32 v157, v114, v113
	v_add_u32_e32 v158, v115, v83
	v_add_u32_e32 v159, v80, v82
	v_add_u32_e32 v160, 64, v78
	v_mov_b32_e32 v96, 0xc604b4df
	v_mov_b32_e32 v95, v94
	v_mov_b32_e32 v98, v94
	v_mov_b32_e32 v99, v94
	v_mov_b32_e32 v100, v94
	v_mov_b32_e32 v101, v94
	v_mov_b32_e32 v102, v94
	v_mov_b32_e32 v103, v94
	v_mov_b32_e32 v104, v94
	v_mov_b32_e32 v105, v94
	v_mov_b32_e32 v106, v94
	v_mov_b32_e32 v107, v94
	v_mov_b32_e32 v108, v94
	v_mov_b32_e32 v109, v94
	v_mov_b32_e32 v110, v94
	v_mov_b32_e32 v111, v94
	v_mov_b32_e32 v112, v94
	v_mov_b32_e32 v113, v94
	v_mov_b32_e32 v114, v94
	v_mov_b32_e32 v115, v94
	v_mov_b32_e32 v117, v94
	s_waitcnt lgkmcnt(0)
	s_barrier
	s_mov_b32 s26, 0x2580
	s_mov_b32 s27, 0x3580
	s_mov_b32 s28, 0x4580
	buffer_load_dwordx4 v[6:9], v192, s[16:19], s26 offen nt
	buffer_load_dwordx4 v[10:13], v192, s[16:19], s26 offen offset:1024 nt
	buffer_load_dwordx4 v[18:21], v192, s[16:19], s26 offen offset:2048 nt
	buffer_load_dwordx4 v[22:25], v192, s[16:19], s26 offen offset:3072 nt
	buffer_load_dwordx4 v[26:29], v192, s[16:19], s27 offen nt
	buffer_load_dwordx4 v[30:33], v192, s[16:19], s27 offen offset:1024 nt
	buffer_load_dwordx4 v[38:41], v192, s[16:19], s27 offen offset:2048 nt
	buffer_load_dwordx4 v[42:45], v192, s[16:19], s27 offen offset:3072 nt
	buffer_load_dwordx4 v[50:53], v192, s[16:19], s28 offen nt
	buffer_load_dwordx4 v[186:189], v193, s[16:19], s26 offen offset:1024 nt
	s_waitcnt vmcnt(25)
	v_cvt_pk_f16_f32 v79, v4, v5
	v_cvt_pk_f16_f32 v78, v2, v3
	ds_write_b64 v141, v[78:79] offset:19456
	s_waitcnt vmcnt(24)
	v_cvt_pk_f16_f32 v79, v16, v17
	v_cvt_pk_f16_f32 v78, v14, v15
	ds_write_b64 v143, v[78:79] offset:19456
	s_waitcnt vmcnt(23)
	v_cvt_pk_f16_f32 v79, v36, v37
	v_cvt_pk_f16_f32 v78, v34, v35
	ds_write_b64 v144, v[78:79] offset:19456
	s_waitcnt vmcnt(22)
	v_cvt_pk_f16_f32 v79, v48, v49
	v_cvt_pk_f16_f32 v78, v46, v47
	ds_write_b64 v145, v[78:79] offset:19456
	s_waitcnt vmcnt(21)
	v_cvt_pk_f16_f32 v79, v56, v57
	v_cvt_pk_f16_f32 v78, v54, v55
	ds_write_b64 v146, v[78:79] offset:19456
	s_waitcnt vmcnt(20)
	v_cvt_pk_f16_f32 v79, v60, v61
	v_cvt_pk_f16_f32 v78, v58, v59
	ds_write_b64 v147, v[78:79] offset:19456
	s_waitcnt vmcnt(19)
	v_cvt_pk_f16_f32 v79, v64, v65
	v_cvt_pk_f16_f32 v78, v62, v63
	ds_write_b64 v141, v[78:79] offset:22568
	s_waitcnt vmcnt(18)
	v_cvt_pk_f16_f32 v79, v68, v69
	v_cvt_pk_f16_f32 v78, v66, v67
	ds_write_b64 v148, v[78:79] offset:19456
	s_waitcnt vmcnt(17)
	v_cvt_pk_f16_f32 v79, v72, v73
	v_cvt_pk_f16_f32 v78, v70, v71
	ds_write_b64 v149, v[78:79] offset:19456
	s_waitcnt vmcnt(16)
	v_cvt_pk_f16_f32 v79, v76, v77
	v_cvt_pk_f16_f32 v78, v74, v75
	s_and_saveexec_b64 s[12:13], s[8:9]
	ds_write_b64 v150, v[78:79] offset:19456
	s_or_b64 exec, exec, s[12:13]
	s_waitcnt vmcnt(10)
	v_cmp_lt_i32_e64 s[30:31], 1, v125
	v_cmp_lt_i32_e64 s[32:33], 1, v190
	v_cmp_lt_i32_e64 s[34:35], 1, v126
	v_cmp_lt_i32_e64 s[36:37], 1, v127
	v_cndmask_b32_e64 v191, 0, 1, s[30:31]
	v_cndmask_b32_e64 v190, 0, 2, s[32:33]
	v_cndmask_b32_e64 v126, 0, 4, s[34:35]
	v_cndmask_b32_e64 v127, 0, 8, s[36:37]
	v_or3_b32 v191, v191, v190, v126
	v_or_b32_e32 v191, v191, v127
	s_mov_b32 s26, 0x4b00
	s_mov_b32 s27, 0x5b00
	s_mov_b32 s28, 0x6b00
	buffer_load_dwordx4 v[2:5], v192, s[16:19], s26 offen nt
	buffer_load_dwordx4 v[14:17], v192, s[16:19], s26 offen offset:1024 nt
	buffer_load_dwordx4 v[34:37], v192, s[16:19], s26 offen offset:2048 nt
	buffer_load_dwordx4 v[46:49], v192, s[16:19], s26 offen offset:3072 nt
	buffer_load_dwordx4 v[54:57], v192, s[16:19], s27 offen nt
	buffer_load_dwordx4 v[58:61], v192, s[16:19], s27 offen offset:1024 nt
	buffer_load_dwordx4 v[62:65], v192, s[16:19], s27 offen offset:2048 nt
	buffer_load_dwordx4 v[66:69], v192, s[16:19], s27 offen offset:3072 nt
	buffer_load_dwordx4 v[70:73], v192, s[16:19], s28 offen nt
	buffer_load_dwordx4 v[74:77], v193, s[16:19], s26 offen offset:1024 nt
	s_mov_b32 s3, 0
	s_branch .LBB0_7
.Lret0:
	s_setprio 2
	s_waitcnt vmcnt(19)
	v_cvt_pk_f16_f32 v79, v8, v9
	v_cvt_pk_f16_f32 v78, v6, v7
	ds_write_b64 v141, v[78:79] offset:19456
	s_waitcnt vmcnt(18)
	v_cvt_pk_f16_f32 v79, v12, v13
	v_cvt_pk_f16_f32 v78, v10, v11
	ds_write_b64 v143, v[78:79] offset:19456
	s_waitcnt vmcnt(17)
	v_cvt_pk_f16_f32 v79, v20, v21
	v_cvt_pk_f16_f32 v78, v18, v19
	ds_write_b64 v144, v[78:79] offset:19456
	s_waitcnt vmcnt(16)
	v_cvt_pk_f16_f32 v79, v24, v25
	v_cvt_pk_f16_f32 v78, v22, v23
	ds_write_b64 v145, v[78:79] offset:19456
	s_waitcnt vmcnt(15)
	v_cvt_pk_f16_f32 v79, v28, v29
	v_cvt_pk_f16_f32 v78, v26, v27
	ds_write_b64 v146, v[78:79] offset:19456
	s_waitcnt vmcnt(14)
	v_cvt_pk_f16_f32 v79, v32, v33
	v_cvt_pk_f16_f32 v78, v30, v31
	ds_write_b64 v147, v[78:79] offset:19456
	s_waitcnt vmcnt(13)
	v_cvt_pk_f16_f32 v79, v40, v41
	v_cvt_pk_f16_f32 v78, v38, v39
	ds_write_b64 v141, v[78:79] offset:22568
	s_waitcnt vmcnt(12)
	v_cvt_pk_f16_f32 v79, v44, v45
	v_cvt_pk_f16_f32 v78, v42, v43
	ds_write_b64 v148, v[78:79] offset:19456
	s_waitcnt vmcnt(11)
	v_cvt_pk_f16_f32 v79, v52, v53
	v_cvt_pk_f16_f32 v78, v50, v51
	ds_write_b64 v149, v[78:79] offset:19456
	s_waitcnt vmcnt(10)
	v_cvt_pk_f16_f32 v79, v188, v189
	v_cvt_pk_f16_f32 v78, v186, v187
	s_and_saveexec_b64 s[12:13], s[8:9]
	ds_write_b64 v150, v[78:79] offset:19456
	s_or_b64 exec, exec, s[12:13]
	s_mov_b32 s26, 0x7080
	s_mov_b32 s27, 0x8080
	s_mov_b32 s28, 0x9080
	buffer_load_dwordx4 v[6:9], v192, s[16:19], s26 offen nt
	buffer_load_dwordx4 v[10:13], v192, s[16:19], s26 offen offset:1024 nt
	buffer_load_dwordx4 v[18:21], v192, s[16:19], s26 offen offset:2048 nt
	buffer_load_dwordx4 v[22:25], v192, s[16:19], s26 offen offset:3072 nt
	buffer_load_dwordx4 v[26:29], v192, s[16:19], s27 offen nt
	buffer_load_dwordx4 v[30:33], v192, s[16:19], s27 offen offset:1024 nt
	buffer_load_dwordx4 v[38:41], v192, s[16:19], s27 offen offset:2048 nt
	buffer_load_dwordx4 v[42:45], v192, s[16:19], s27 offen offset:3072 nt
	buffer_load_dwordx4 v[50:53], v192, s[16:19], s28 offen nt
	buffer_load_dwordx4 v[186:189], v193, s[16:19], s26 offen offset:1024 nt
	s_mov_b32 s3, 1
	s_branch .LBB0_7
.Lret1:
	s_setprio 1
	s_waitcnt vmcnt(19)
	v_cvt_pk_f16_f32 v79, v4, v5
	v_cvt_pk_f16_f32 v78, v2, v3
	ds_write_b64 v141, v[78:79] offset:19456
	s_waitcnt vmcnt(18)
	v_cvt_pk_f16_f32 v79, v16, v17
	v_cvt_pk_f16_f32 v78, v14, v15
	ds_write_b64 v143, v[78:79] offset:19456
	s_waitcnt vmcnt(17)
	v_cvt_pk_f16_f32 v79, v36, v37
	v_cvt_pk_f16_f32 v78, v34, v35
	ds_write_b64 v144, v[78:79] offset:19456
	s_waitcnt vmcnt(16)
	v_cvt_pk_f16_f32 v79, v48, v49
	v_cvt_pk_f16_f32 v78, v46, v47
	ds_write_b64 v145, v[78:79] offset:19456
	s_waitcnt vmcnt(15)
	v_cvt_pk_f16_f32 v79, v56, v57
	v_cvt_pk_f16_f32 v78, v54, v55
	ds_write_b64 v146, v[78:79] offset:19456
	s_waitcnt vmcnt(14)
	v_cvt_pk_f16_f32 v79, v60, v61
	v_cvt_pk_f16_f32 v78, v58, v59
	ds_write_b64 v147, v[78:79] offset:19456
	s_waitcnt vmcnt(13)
	v_cvt_pk_f16_f32 v79, v64, v65
	v_cvt_pk_f16_f32 v78, v62, v63
	ds_write_b64 v141, v[78:79] offset:22568
	s_waitcnt vmcnt(12)
	v_cvt_pk_f16_f32 v79, v68, v69
	v_cvt_pk_f16_f32 v78, v66, v67
	ds_write_b64 v148, v[78:79] offset:19456
	s_waitcnt vmcnt(11)
	v_cvt_pk_f16_f32 v79, v72, v73
	v_cvt_pk_f16_f32 v78, v70, v71
	ds_write_b64 v149, v[78:79] offset:19456
	s_waitcnt vmcnt(10)
	v_cvt_pk_f16_f32 v79, v76, v77
	v_cvt_pk_f16_f32 v78, v74, v75
	s_and_saveexec_b64 s[12:13], s[8:9]
	ds_write_b64 v150, v[78:79] offset:19456
	s_or_b64 exec, exec, s[12:13]
	s_mov_b32 s3, 2
	s_branch .LBB0_7
.Lret2:
	s_setprio 0
	v_lshrrev_b32_e32 v151, 4, v120
	v_lshl_add_u32 v152, v123, 4, v131
	v_lshlrev_b32_e32 v153, 4, v123
	v_lshlrev_b32_e32 v154, 1, v121
	v_lshrrev_b32_e32 v155, 4, v122
	v_lshl_add_u32 v152, v151, 2, v152
	v_or_b32_e32 v155, v154, v155
	v_sub_u32_e32 v174, 11, v154
	v_lshl_or_b32 v156, v155, 8, v153
	v_cvt_f32_i32_e32 v174, v174
	v_cmp_lt_u32_e32 vcc, 31, v0
	v_add_u32_e32 v157, 0x4c00, v156
	v_mul_f32_e32 v175, 0xbf38aa3b, v174
	v_add_u32_e32 v158, 0xe400, v156
	v_mul_f32_e32 v175, v175, v174
	v_exp_f32_e32 v175, v175
	s_nop 0
	v_cndmask_b32_e32 v174, 1.0, v175, vcc
	s_waitcnt vmcnt(9)
	v_cvt_pk_f16_f32 v79, v8, v9
	v_cvt_pk_f16_f32 v78, v6, v7
	ds_write_b64 v141, v[78:79] offset:19456
	s_waitcnt vmcnt(8)
	v_cvt_pk_f16_f32 v79, v12, v13
	v_cvt_pk_f16_f32 v78, v10, v11
	ds_write_b64 v143, v[78:79] offset:19456
	s_waitcnt vmcnt(7)
	v_cvt_pk_f16_f32 v79, v20, v21
	v_cvt_pk_f16_f32 v78, v18, v19
	ds_write_b64 v144, v[78:79] offset:19456
	s_waitcnt vmcnt(6)
	v_cvt_pk_f16_f32 v79, v24, v25
	v_cvt_pk_f16_f32 v78, v22, v23
	ds_write_b64 v145, v[78:79] offset:19456
	s_waitcnt vmcnt(5)
	v_cvt_pk_f16_f32 v79, v28, v29
	v_cvt_pk_f16_f32 v78, v26, v27
	ds_write_b64 v146, v[78:79] offset:19456
	s_waitcnt vmcnt(4)
	v_cvt_pk_f16_f32 v79, v32, v33
	v_cvt_pk_f16_f32 v78, v30, v31
	ds_write_b64 v147, v[78:79] offset:19456
	s_waitcnt vmcnt(3)
	v_cvt_pk_f16_f32 v79, v40, v41
	v_cvt_pk_f16_f32 v78, v38, v39
	ds_write_b64 v141, v[78:79] offset:22568
	s_waitcnt vmcnt(2)
	v_cvt_pk_f16_f32 v79, v44, v45
	v_cvt_pk_f16_f32 v78, v42, v43
	ds_write_b64 v148, v[78:79] offset:19456
	s_waitcnt vmcnt(1)
	v_cvt_pk_f16_f32 v79, v52, v53
	v_cvt_pk_f16_f32 v78, v50, v51
	ds_write_b64 v149, v[78:79] offset:19456
	s_mov_b32 s3, 3
	v_mov_b32_e32 v86, 0
	v_mov_b32_e32 v78, 0
	v_mov_b32_e32 v79, 0
	v_mov_b32_e32 v80, 0
	v_mov_b32_e32 v81, 0
	v_mov_b32_e32 v82, 0
	v_mov_b32_e32 v83, 0
	v_mov_b32_e32 v84, 0
	v_mov_b32_e32 v85, 0
	ds_read_b128 v[194:197], v142
	ds_read_b128 v[198:201], v136
	ds_read_b128 v[202:205], v136 offset:9728
	ds_read_b128 v[206:209], v142 offset:64
	ds_read_b128 v[210:213], v136 offset:64
	ds_read_b128 v[214:217], v136 offset:9792
	ds_read_b128 v[218:221], v142 offset:128
	ds_read_b128 v[222:225], v136 offset:128
	ds_read_b128 v[226:229], v136 offset:9856
	ds_read_b128 v[230:233], v142 offset:192
	ds_read_b128 v[234:237], v136 offset:192
	ds_read_b128 v[238:241], v136 offset:9920
	s_waitcnt lgkmcnt(9)
	v_mfma_f32_16x16x32_f16 v[78:81], v[194:197], v[198:201], v[78:81]
	v_dot2c_f32_f16_e32 v86, v194, v194
	v_dot2c_f32_f16_e32 v86, v195, v195
	v_mfma_f32_16x16x32_f16 v[82:85], v[194:197], v[202:205], v[82:85]
	v_dot2c_f32_f16_e32 v86, v196, v196
	v_dot2c_f32_f16_e32 v86, v197, v197
	ds_read_b128 v[194:197], v142 offset:256
	ds_read_b128 v[198:201], v136 offset:256
	ds_read_b128 v[202:205], v136 offset:9984
	s_waitcnt lgkmcnt(9)
	v_mfma_f32_16x16x32_f16 v[78:81], v[206:209], v[210:213], v[78:81]
	v_dot2c_f32_f16_e32 v86, v206, v206
	v_dot2c_f32_f16_e32 v86, v207, v207
	v_mfma_f32_16x16x32_f16 v[82:85], v[206:209], v[214:217], v[82:85]
	v_dot2c_f32_f16_e32 v86, v208, v208
	v_dot2c_f32_f16_e32 v86, v209, v209
	ds_read_b128 v[206:209], v142 offset:320
	ds_read_b128 v[210:213], v136 offset:320
	ds_read_b128 v[214:217], v136 offset:10048
	s_waitcnt lgkmcnt(9)
	v_mfma_f32_16x16x32_f16 v[78:81], v[218:221], v[222:225], v[78:81]
	v_dot2c_f32_f16_e32 v86, v218, v218
	v_dot2c_f32_f16_e32 v86, v219, v219
	v_mfma_f32_16x16x32_f16 v[82:85], v[218:221], v[226:229], v[82:85]
	v_dot2c_f32_f16_e32 v86, v220, v220
	v_dot2c_f32_f16_e32 v86, v221, v221
	s_waitcnt lgkmcnt(6)
	v_mfma_f32_16x16x32_f16 v[78:81], v[230:233], v[234:237], v[78:81]
	v_dot2c_f32_f16_e32 v86, v230, v230
	v_dot2c_f32_f16_e32 v86, v231, v231
	v_mfma_f32_16x16x32_f16 v[82:85], v[230:233], v[238:241], v[82:85]
	v_dot2c_f32_f16_e32 v86, v232, v232
	v_dot2c_f32_f16_e32 v86, v233, v233
	s_waitcnt lgkmcnt(3)
	v_mfma_f32_16x16x32_f16 v[78:81], v[194:197], v[198:201], v[78:81]
	v_dot2c_f32_f16_e32 v86, v194, v194
	v_dot2c_f32_f16_e32 v86, v195, v195
	v_mfma_f32_16x16x32_f16 v[82:85], v[194:197], v[202:205], v[82:85]
	v_dot2c_f32_f16_e32 v86, v196, v196
	v_dot2c_f32_f16_e32 v86, v197, v197
	s_waitcnt lgkmcnt(0)
	v_mfma_f32_16x16x32_f16 v[78:81], v[206:209], v[210:213], v[78:81]
	v_dot2c_f32_f16_e32 v86, v206, v206
	v_dot2c_f32_f16_e32 v86, v207, v207
	v_mfma_f32_16x16x32_f16 v[82:85], v[206:209], v[214:217], v[82:85]
	v_dot2c_f32_f16_e32 v86, v208, v208
	v_dot2c_f32_f16_e32 v86, v209, v209
	ds_read_b128 v[222:225], v136 offset:384
	ds_read_b128 v[226:229], v136 offset:10112
	ds_read_b128 v[234:237], v136 offset:448
	ds_read_b128 v[238:241], v136 offset:10176
	ds_read_b128 v[198:201], v136 offset:512
	ds_read_b128 v[202:205], v136 offset:10240
	ds_read2st64_b64 v[88:91], v160 offset0:1 offset1:20
	s_waitcnt vmcnt(0)
	v_cvt_pk_f16_f32 v163, v188, v189
	v_cvt_pk_f16_f32 v162, v186, v187
	s_and_saveexec_b64 s[12:13], s[8:9]
	ds_write_b64 v150, v[162:163] offset:19456
	s_or_b64 exec, exec, s[12:13]
	ds_read_b128 v[218:221], v142 offset:384
	ds_read_b128 v[230:233], v142 offset:448
	ds_read_b128 v[194:197], v142 offset:512
	ds_read_b64 v[92:93], v159 offset:20032
	s_waitcnt lgkmcnt(3)
	v_mfma_f32_16x16x32_f16 v[78:81], v[218:221], v[222:225], v[78:81]
	v_dot2c_f32_f16_e32 v86, v218, v218
	v_dot2c_f32_f16_e32 v86, v219, v219
	v_mfma_f32_16x16x32_f16 v[82:85], v[218:221], v[226:229], v[82:85]
	v_dot2c_f32_f16_e32 v86, v220, v220
	v_dot2c_f32_f16_e32 v86, v221, v221
	s_waitcnt lgkmcnt(2)
	v_mfma_f32_16x16x32_f16 v[78:81], v[230:233], v[234:237], v[78:81]
	v_dot2c_f32_f16_e32 v86, v230, v230
	v_dot2c_f32_f16_e32 v86, v231, v231
	v_mfma_f32_16x16x32_f16 v[82:85], v[230:233], v[238:241], v[82:85]
	v_dot2c_f32_f16_e32 v86, v232, v232
	v_dot2c_f32_f16_e32 v86, v233, v233
	s_waitcnt lgkmcnt(1)
	v_mfma_f32_16x16x32_f16 v[78:81], v[194:197], v[198:201], v[78:81]
	v_dot2c_f32_f16_e32 v86, v194, v194
	v_dot2c_f32_f16_e32 v86, v195, v195
	v_mfma_f32_16x16x32_f16 v[82:85], v[194:197], v[202:205], v[82:85]
	v_dot2c_f32_f16_e32 v86, v196, v196
	v_dot2c_f32_f16_e32 v86, v197, v197
	s_waitcnt lgkmcnt(0)
	v_mfma_f32_16x16x16_f16 v[78:81], v[92:93], v[88:89], v[78:81]
	v_dot2c_f32_f16_e32 v86, v92, v92
	v_dot2c_f32_f16_e32 v86, v93, v93
	v_mfma_f32_16x16x16_f16 v[82:85], v[92:93], v[90:91], v[82:85]
	s_branch .Lnorm
